# speedup vs baseline: 1.0471x; 1.0054x over previous
_Z9tg_kernelILi64ELi8ELi1ELb0EEvPKDF16_iS1_iPviPKf:
	s_load_dwordx2 s[4:5], s[0:1], 0x0
	s_load_dword s7, s[0:1], 0x8
	s_load_dwordx2 s[12:13], s[0:1], 0x10
	s_load_dword s6, s[0:1], 0x18
	v_readfirstlane_b32 s9, v0
	s_lshr_b32 s8, s9, 6
	s_lshl_b32 s10, s3, 6
	s_lshl_b32 s11, s2, 7
	v_bfe_u32 v1, v0, 3, 3
	v_bitop3_b32 v8, v1, v0, 7 bitop3:0x78
	v_or_b32_e32 v2, s10, v1
	s_lshl_b32 s14, s8, 3
	v_or_b32_e32 v1, s11, v1
	v_add_u32_e32 v1, s14, v1
	s_waitcnt lgkmcnt(0)
	v_mad_i64_i32 v[4:5], s[2:3], v1, s6, 0
	v_add_u32_e32 v2, s14, v2
	v_lshl_add_u64 v[6:7], v[4:5], 1, s[12:13]
	v_lshlrev_b32_e32 v4, 4, v8
	v_mov_b32_e32 v5, 0
	v_add_u32_e32 v1, 64, v1
	v_mad_i64_i32 v[2:3], s[2:3], v2, s7, 0
	v_lshl_add_u64 v[50:51], v[6:7], 0, v[4:5]
	v_mad_i64_i32 v[6:7], s[2:3], v1, s6, 0
	s_lshl_b32 s2, s8, 10
	v_lshl_add_u64 v[2:3], v[2:3], 1, s[4:5]
	s_add_i32 s14, s2, 0
	v_lshl_add_u64 v[54:55], v[2:3], 0, v[4:5]
	s_mov_b32 m0, s14
	v_lshl_add_u64 v[6:7], v[6:7], 1, s[12:13]
	global_load_lds_dwordx4 v[54:55], off
	s_add_i32 m0, s14, 0x2000
	v_lshl_add_u64 v[52:53], v[6:7], 0, v[4:5]
	global_load_lds_dwordx4 v[50:51], off
	s_add_i32 m0, s14, 0x4000
	s_ashr_i32 s7, s6, 31
	global_load_lds_dwordx4 v[52:53], off
	v_mov_b64_e32 v[2:3], 0x80
	v_cmp_lt_i64_e32 vcc, s[6:7], v[2:3]
	s_mov_b64 s[2:3], 0x80
	v_and_b32_e32 v2, 63, v0
	s_cbranch_vccnz .LBB10_2
	v_lshl_add_u64 v[6:7], v[54:55], 0, s[2:3]
	s_add_i32 m0, s14, 0x6000
	s_nop 0
	global_load_lds_dwordx4 v[6:7], off
	s_add_i32 m0, s14, 0x8000
	v_lshl_add_u64 v[6:7], v[50:51], 0, s[2:3]
	global_load_lds_dwordx4 v[6:7], off
	v_lshl_add_u64 v[6:7], v[52:53], 0, s[2:3]
	s_add_i32 m0, s14, 0xa000
	s_nop 0
	global_load_lds_dwordx4 v[6:7], off
	s_mov_b64 s[2:3], 256
	v_lshl_add_u64 v[6:7], v[54:55], 0, s[2:3]
	s_add_i32 m0, s14, 0xc000
	s_nop 0
	global_load_lds_dwordx4 v[6:7], off
	s_add_i32 m0, s14, 0xe000
	v_lshl_add_u64 v[6:7], v[50:51], 0, s[2:3]
	global_load_lds_dwordx4 v[6:7], off
	v_lshl_add_u64 v[6:7], v[52:53], 0, s[2:3]
	s_add_i32 m0, s14, 0x10000
	s_nop 0
	global_load_lds_dwordx4 v[6:7], off
	s_mov_b64 s[2:3], 384
	v_lshl_add_u64 v[6:7], v[54:55], 0, s[2:3]
	s_add_i32 m0, s14, 0x12000
	s_nop 0
	global_load_lds_dwordx4 v[6:7], off
	s_add_i32 m0, s14, 0x14000
	v_lshl_add_u64 v[6:7], v[50:51], 0, s[2:3]
	global_load_lds_dwordx4 v[6:7], off
	v_lshl_add_u64 v[6:7], v[52:53], 0, s[2:3]
	s_add_i32 m0, s14, 0x16000
	s_nop 0
	global_load_lds_dwordx4 v[6:7], off
.LBB10_2:
	s_load_dwordx2 s[2:3], s[0:1], 0x20
	s_load_dwordx2 s[4:5], s[0:1], 0x30
	s_lshr_b32 s12, s9, 8
	s_and_b32 s13, s8, 3
	v_and_b32_e32 v1, 15, v0
	v_lshrrev_b32_e32 v56, 4, v2
	s_cmp_lt_i32 s6, 64
	v_mov_b32_e32 v4, 0
	v_mov_b32_e32 v3, 0
	v_mov_b32_e32 v2, 0
	v_mov_b32_e32 v17, 0
	v_mov_b32_e32 v16, 0
	v_mov_b32_e32 v15, 0
	v_mov_b32_e32 v14, 0
	v_mov_b32_e32 v9, 0
	v_mov_b32_e32 v8, 0
	v_mov_b32_e32 v7, 0
	v_mov_b32_e32 v6, 0
	v_mov_b32_e32 v13, 0
	v_mov_b32_e32 v12, 0
	v_mov_b32_e32 v11, 0
	v_mov_b32_e32 v10, 0
	s_cbranch_scc1 .LBB10_11
	v_and_b32_e32 v2, 7, v0
	s_lshr_b32 s7, s7, 26
	v_xor_b32_e32 v0, v56, v2
	v_lshlrev_b32_e32 v3, 7, v1
	v_bitop3_b32 v2, v56, v2, 4 bitop3:0x36
	s_add_i32 s6, s6, s7
	v_mov_b32_e32 v10, 0
	s_mov_b32 s7, 0
	v_lshlrev_b32_e32 v0, 4, v0
	v_lshl_or_b32 v57, s12, 12, v3
	v_lshlrev_b32_e32 v58, 4, v2
	v_lshl_or_b32 v59, s13, 12, v3
	s_ashr_i32 s15, s6, 6
	s_movk_i32 s6, 0x80
	s_mov_b32 s18, s7
	s_mov_b32 s16, s7
	v_mov_b32_e32 v11, v10
	v_mov_b32_e32 v12, v10
	v_mov_b32_e32 v13, v10
	v_mov_b32_e32 v6, v10
	v_mov_b32_e32 v7, v10
	v_mov_b32_e32 v8, v10
	v_mov_b32_e32 v9, v10
	v_mov_b32_e32 v14, v10
	v_mov_b32_e32 v15, v10
	v_mov_b32_e32 v16, v10
	v_mov_b32_e32 v17, v10
	v_mov_b32_e32 v2, v10
	v_mov_b32_e32 v3, v10
	v_mov_b32_e32 v4, v10
	v_mov_b32_e32 v5, v10
	s_mov_b32 s20, 0
	s_mov_b32 s21, 0
	s_mov_b32 s24, 512
	s_mov_b32 s25, 0
.Ltk10_top:
	s_add_i32 s22, s20, 2
	s_cmp_ge_i32 s22, s15
	s_cbranch_scc1 .Ltk10_w0
	s_waitcnt vmcnt(6)
	s_branch .Ltk10_wd

.Ltk10_wd:
	s_mov_b32 s9, s21
	s_add_i32 s23, s21, 0x6000
	s_barrier
	v_add_u32_e32 v26, s9, v0
	v_add_u32_e32 v42, s9, v58
	v_add_u32_e32 v18, v26, v57
	v_add_u32_e32 v30, v26, v59
	v_add_u32_e32 v34, v42, v57
	v_add_u32_e32 v46, v42, v59
	ds_read_b128 v[22:25], v18
	ds_read_b128 v[18:21], v18 offset:2048
	ds_read_b128 v[26:29], v30 offset:8192
	ds_read_b128 v[30:33], v30 offset:10240
	ds_read_b128 v[38:41], v34
	ds_read_b128 v[34:37], v34 offset:2048
	ds_read_b128 v[42:45], v46 offset:8192
	ds_read_b128 v[46:49], v46 offset:10240
	v_add_u32_e32 v90, s23, v0
	v_add_u32_e32 v106, s23, v58
	v_add_u32_e32 v82, v90, v57
	v_add_u32_e32 v94, v90, v59
	v_add_u32_e32 v98, v106, v57
	v_add_u32_e32 v110, v106, v59
	ds_read_b128 v[86:89], v82
	ds_read_b128 v[82:85], v82 offset:2048
	ds_read_b128 v[90:93], v94 offset:8192
	ds_read_b128 v[94:97], v94 offset:10240
	ds_read_b128 v[102:105], v98
	ds_read_b128 v[98:101], v98 offset:2048
	ds_read_b128 v[106:109], v110 offset:8192
	ds_read_b128 v[110:113], v110 offset:10240
	s_add_i32 s22, s20, 4
	s_cmp_ge_i32 s22, s15
	s_cbranch_scc1 .Ltk10_noi
	s_add_i32 s26, s21, 0x18000
	s_cmp_ge_u32 s26, 0x24000
	s_cbranch_scc0 .Ltk10_nw
	s_sub_i32 s26, s26, 0x24000
.Ltk10_nw:
	v_lshl_add_u64 v[60:61], v[54:55], 0, s[24:25]
	s_add_i32 m0, s14, s26
	s_nop 0
	global_load_lds_dwordx4 v[60:61], off
	s_add_i32 s27, s26, 0x2000
	v_lshl_add_u64 v[60:61], v[50:51], 0, s[24:25]
	s_add_i32 m0, s14, s27
	s_nop 0
	global_load_lds_dwordx4 v[60:61], off
	s_add_i32 s27, s26, 0x4000
	v_lshl_add_u64 v[60:61], v[52:53], 0, s[24:25]
	s_add_i32 m0, s14, s27
	s_nop 0
	global_load_lds_dwordx4 v[60:61], off
	s_add_u32 s28, s24, 128
	s_addc_u32 s29, s25, 0
	s_add_i32 s26, s26, 0x6000
	v_lshl_add_u64 v[60:61], v[54:55], 0, s[28:29]
	s_add_i32 m0, s14, s26
	s_nop 0
	global_load_lds_dwordx4 v[60:61], off
	s_add_i32 s27, s26, 0x2000
	v_lshl_add_u64 v[60:61], v[50:51], 0, s[28:29]
	s_add_i32 m0, s14, s27
	s_nop 0
	global_load_lds_dwordx4 v[60:61], off
	s_add_i32 s27, s26, 0x4000
	v_lshl_add_u64 v[60:61], v[52:53], 0, s[28:29]
	s_add_i32 m0, s14, s27
	s_nop 0
	global_load_lds_dwordx4 v[60:61], off
.Ltk10_noi:
	s_setprio 1
	s_waitcnt lgkmcnt(0)
	v_mfma_f32_16x16x32_f16 v[10:13], v[26:29], v[22:25], v[10:13]
	v_mfma_f32_16x16x32_f16 v[6:9], v[30:33], v[22:25], v[6:9]
	v_mfma_f32_16x16x32_f16 v[14:17], v[26:29], v[18:21], v[14:17]
	v_mfma_f32_16x16x32_f16 v[2:5], v[30:33], v[18:21], v[2:5]
	v_mfma_f32_16x16x32_f16 v[10:13], v[42:45], v[38:41], v[10:13]
	v_mfma_f32_16x16x32_f16 v[6:9], v[46:49], v[38:41], v[6:9]
	v_mfma_f32_16x16x32_f16 v[14:17], v[42:45], v[34:37], v[14:17]
	v_mfma_f32_16x16x32_f16 v[2:5], v[46:49], v[34:37], v[2:5]
	v_mfma_f32_16x16x32_f16 v[10:13], v[90:93], v[86:89], v[10:13]
	v_mfma_f32_16x16x32_f16 v[6:9], v[94:97], v[86:89], v[6:9]
	v_mfma_f32_16x16x32_f16 v[14:17], v[90:93], v[82:85], v[14:17]
	v_mfma_f32_16x16x32_f16 v[2:5], v[94:97], v[82:85], v[2:5]
	v_mfma_f32_16x16x32_f16 v[10:13], v[106:109], v[102:105], v[10:13]
	v_mfma_f32_16x16x32_f16 v[6:9], v[110:113], v[102:105], v[6:9]
	v_mfma_f32_16x16x32_f16 v[14:17], v[106:109], v[98:101], v[14:17]
	v_mfma_f32_16x16x32_f16 v[2:5], v[110:113], v[98:101], v[2:5]
	s_setprio 0
	s_add_i32 s21, s21, 0xc000
	s_cmp_ge_u32 s21, 0x24000
	s_cbranch_scc0 .Ltk10_ns
	s_mov_b32 s21, 0
.Ltk10_ns:
	s_add_u32 s24, s24, 256
	s_add_i32 s20, s20, 2
	s_cmp_lt_i32 s20, s15
	s_cbranch_scc1 .Ltk10_top

	.amdhsa_kernel _Z9tg_kernelILi64ELi8ELi1ELb0EEvPKDF16_iS1_iPviPKf
		.amdhsa_group_segment_fixed_size 73728
		.amdhsa_private_segment_fixed_size 0
		.amdhsa_kernarg_size 56
		.amdhsa_user_sgpr_count 2
		.amdhsa_user_sgpr_dispatch_ptr 0
		.amdhsa_user_sgpr_queue_ptr 0
		.amdhsa_user_sgpr_kernarg_segment_ptr 1
		.amdhsa_user_sgpr_dispatch_id 0
		.amdhsa_user_sgpr_kernarg_preload_length 0
		.amdhsa_user_sgpr_kernarg_preload_offset 0
		.amdhsa_user_sgpr_private_segment_size 0
		.amdhsa_uses_dynamic_stack 0
		.amdhsa_enable_private_segment 0
		.amdhsa_system_sgpr_workgroup_id_x 1
		.amdhsa_system_sgpr_workgroup_id_y 1
		.amdhsa_system_sgpr_workgroup_id_z 0
		.amdhsa_system_sgpr_workgroup_info 0
		.amdhsa_system_vgpr_workitem_id 0
		.amdhsa_next_free_vgpr 128
		.amdhsa_next_free_sgpr 32
		.amdhsa_accum_offset 128
		.amdhsa_reserve_vcc 1
		.amdhsa_float_round_mode_32 0
		.amdhsa_float_round_mode_16_64 0
		.amdhsa_float_denorm_mode_32 3
		.amdhsa_float_denorm_mode_16_64 3
		.amdhsa_dx10_clamp 1
		.amdhsa_ieee_mode 1
		.amdhsa_fp16_overflow 0
		.amdhsa_tg_split 0
		.amdhsa_exception_fp_ieee_invalid_op 0
		.amdhsa_exception_fp_denorm_src 0
		.amdhsa_exception_fp_ieee_div_zero 0
		.amdhsa_exception_fp_ieee_overflow 0
		.amdhsa_exception_fp_ieee_underflow 0
		.amdhsa_exception_fp_ieee_inexact 0
		.amdhsa_exception_int_div_zero 0
	.end_amdhsa_kernel

amdhsa.kernels:
  - .agpr_count:     0
    .args:
      - .offset:         0
        .size:           32
        .value_kind:     by_value
      - .address_space:  global
        .offset:         32
        .size:           8
        .value_kind:     global_buffer
      - .address_space:  global
        .offset:         40
        .size:           8
        .value_kind:     global_buffer
      - .offset:         48
        .size:           4
        .value_kind:     by_value
      - .offset:         56
        .size:           4
        .value_kind:     hidden_block_count_x
      - .offset:         60
        .size:           4
        .value_kind:     hidden_block_count_y
      - .offset:         64
        .size:           4
        .value_kind:     hidden_block_count_z
      - .offset:         68
        .size:           2
        .value_kind:     hidden_group_size_x
      - .offset:         70
        .size:           2
        .value_kind:     hidden_group_size_y
      - .offset:         72
        .size:           2
        .value_kind:     hidden_group_size_z
      - .offset:         74
        .size:           2
        .value_kind:     hidden_remainder_x
      - .offset:         76
        .size:           2
        .value_kind:     hidden_remainder_y
      - .offset:         78
        .size:           2
        .value_kind:     hidden_remainder_z
      - .offset:         96
        .size:           8
        .value_kind:     hidden_global_offset_x
      - .offset:         104
        .size:           8
        .value_kind:     hidden_global_offset_y
      - .offset:         112
        .size:           8
        .value_kind:     hidden_global_offset_z
      - .offset:         120
        .size:           2
        .value_kind:     hidden_grid_dims
      - .offset:         176
        .size:           4
        .value_kind:     hidden_dynamic_lds_size
    .group_segment_fixed_size: 0
    .kernarg_segment_align: 8
    .kernarg_segment_size: 312
    .language:       OpenCL C
    .language_version:
      - 2
      - 0
    .max_flat_workgroup_size: 512
    .name:           _Z10k_phase_hmN3pg84GemmEPDF16_PKfi
    .private_segment_fixed_size: 0
    .sgpr_count:     68
    .sgpr_spill_count: 0
    .symbol:         _Z10k_phase_hmN3pg84GemmEPDF16_PKfi.kd
    .uniform_work_group_size: 1
    .uses_dynamic_stack: false
    .vgpr_count:     140
    .vgpr_spill_count: 0
    .wavefront_size: 64
  - .agpr_count:     0
    .args:
      - .offset:         0
        .size:           32
        .value_kind:     by_value
      - .address_space:  global
        .offset:         32
        .size:           8
        .value_kind:     global_buffer
      - .address_space:  global
        .offset:         40
        .size:           8
        .value_kind:     global_buffer
      - .offset:         48
        .size:           4
        .value_kind:     by_value
      - .offset:         56
        .size:           4
        .value_kind:     hidden_block_count_x
      - .offset:         60
        .size:           4
        .value_kind:     hidden_block_count_y
      - .offset:         64
        .size:           4
        .value_kind:     hidden_block_count_z
      - .offset:         68
        .size:           2
        .value_kind:     hidden_group_size_x
      - .offset:         70
        .size:           2
        .value_kind:     hidden_group_size_y
      - .offset:         72
        .size:           2
        .value_kind:     hidden_group_size_z
      - .offset:         74
        .size:           2
        .value_kind:     hidden_remainder_x
      - .offset:         76
        .size:           2
        .value_kind:     hidden_remainder_y
      - .offset:         78
        .size:           2
        .value_kind:     hidden_remainder_z
      - .offset:         96
        .size:           8
        .value_kind:     hidden_global_offset_x
      - .offset:         104
        .size:           8
        .value_kind:     hidden_global_offset_y
      - .offset:         112
        .size:           8
        .value_kind:     hidden_global_offset_z
      - .offset:         120
        .size:           2
        .value_kind:     hidden_grid_dims
      - .offset:         176
        .size:           4
        .value_kind:     hidden_dynamic_lds_size
    .group_segment_fixed_size: 0
    .kernarg_segment_align: 8
    .kernarg_segment_size: 312
    .language:       OpenCL C
    .language_version:
      - 2
      - 0
    .max_flat_workgroup_size: 512
    .name:           _Z10k_phase_qmN3pg84GemmEPDF16_PKfi
    .private_segment_fixed_size: 0
    .sgpr_count:     67
    .sgpr_spill_count: 0
    .symbol:         _Z10k_phase_qmN3pg84GemmEPDF16_PKfi.kd
    .uniform_work_group_size: 1
    .uses_dynamic_stack: false
    .vgpr_count:     102
    .vgpr_spill_count: 0
    .wavefront_size: 64
  - .agpr_count:     0
    .args:
      - .offset:         0
        .size:           288
        .value_kind:     by_value
    .group_segment_fixed_size: 16640
    .kernarg_segment_align: 8
    .kernarg_segment_size: 288
    .language:       OpenCL C
    .language_version:
      - 2
      - 0
    .max_flat_workgroup_size: 256
    .name:           _Z11prep_kernel8PrepArgs
    .private_segment_fixed_size: 0
    .sgpr_count:     26
    .sgpr_spill_count: 0
    .symbol:         _Z11prep_kernel8PrepArgs.kd
    .uniform_work_group_size: 1
    .uses_dynamic_stack: false
    .vgpr_count:     35
    .vgpr_spill_count: 0
    .wavefront_size: 64
  - .agpr_count:     0
    .args:
      - .actual_access:  read_only
        .address_space:  global
        .offset:         0
        .size:           8
        .value_kind:     global_buffer
      - .actual_access:  read_only
        .address_space:  global
        .offset:         8
        .size:           8
        .value_kind:     global_buffer
      - .actual_access:  read_only
        .address_space:  global
        .offset:         16
        .size:           8
        .value_kind:     global_buffer
      - .actual_access:  write_only
        .address_space:  global
        .offset:         24
        .size:           8
        .value_kind:     global_buffer
    .group_segment_fixed_size: 0
    .kernarg_segment_align: 8
    .kernarg_segment_size: 32
    .language:       OpenCL C
    .language_version:
      - 2
      - 0
    .max_flat_workgroup_size: 256
    .name:           _Z11leaf_kernelPKfS0_PKiPDF16_
    .private_segment_fixed_size: 0
    .sgpr_count:     18
    .sgpr_spill_count: 0
    .symbol:         _Z11leaf_kernelPKfS0_PKiPDF16_.kd
    .uniform_work_group_size: 1
    .uses_dynamic_stack: false
    .vgpr_count:     25
    .vgpr_spill_count: 0
    .wavefront_size: 64
  - .agpr_count:     248
    .args:
      - .actual_access:  read_only
        .address_space:  global
        .offset:         0
        .size:           8
        .value_kind:     global_buffer
      - .actual_access:  read_only
        .address_space:  global
        .offset:         8
        .size:           8
        .value_kind:     global_buffer
      - .actual_access:  write_only
        .address_space:  global
        .offset:         16
        .size:           8
        .value_kind:     global_buffer
      - .actual_access:  write_only
        .address_space:  global
        .offset:         24
        .size:           8
        .value_kind:     global_buffer
    .group_segment_fixed_size: 0
    .kernarg_segment_align: 8
    .kernarg_segment_size: 32
    .language:       OpenCL C
    .language_version:
      - 2
      - 0
    .max_flat_workgroup_size: 256
    .name:           _Z10rnn_kernelPKDF16_S0_PDF16_S1_
    .private_segment_fixed_size: 0
    .sgpr_count:     22
    .sgpr_spill_count: 0
    .symbol:         _Z10rnn_kernelPKDF16_S0_PDF16_S1_.kd
    .uniform_work_group_size: 1
    .uses_dynamic_stack: false
    .vgpr_count:     496
    .vgpr_spill_count: 0
    .wavefront_size: 64
  - .agpr_count:     0
    .args:
      - .actual_access:  read_only
        .address_space:  global
        .offset:         0
        .size:           8
        .value_kind:     global_buffer
      - .actual_access:  read_only
        .address_space:  global
        .offset:         8
        .size:           8
        .value_kind:     global_buffer
      - .actual_access:  write_only
        .address_space:  global
        .offset:         16
        .size:           8
        .value_kind:     global_buffer
    .group_segment_fixed_size: 0
    .kernarg_segment_align: 8
    .kernarg_segment_size: 24
    .language:       OpenCL C
    .language_version:
      - 2
      - 0
    .max_flat_workgroup_size: 256
    .name:           _Z10max_kernelPKDF16_S0_PDF16_
    .private_segment_fixed_size: 0
    .sgpr_count:     18
    .sgpr_spill_count: 0
    .symbol:         _Z10max_kernelPKDF16_S0_PDF16_.kd
    .uniform_work_group_size: 1
    .uses_dynamic_stack: false
    .vgpr_count:     38
    .vgpr_spill_count: 0
    .wavefront_size: 64
  - .agpr_count:     0
    .args:
      - .actual_access:  read_only
        .address_space:  global
        .offset:         0
        .size:           8
        .value_kind:     global_buffer
      - .actual_access:  read_only
        .address_space:  global
        .offset:         8
        .size:           8
        .value_kind:     global_buffer
      - .actual_access:  read_only
        .address_space:  global
        .offset:         16
        .size:           8
        .value_kind:     global_buffer
      - .actual_access:  write_only
        .address_space:  global
        .offset:         24
        .size:           8
        .value_kind:     global_buffer
    .group_segment_fixed_size: 0
    .kernarg_segment_align: 8
    .kernarg_segment_size: 32
    .language:       OpenCL C
    .language_version:
      - 2
      - 0
    .max_flat_workgroup_size: 256
    .name:           _Z12final_kernelPKfS0_S0_Pf
    .private_segment_fixed_size: 0
    .sgpr_count:     14
    .sgpr_spill_count: 0
    .symbol:         _Z12final_kernelPKfS0_S0_Pf.kd
    .uniform_work_group_size: 1
    .uses_dynamic_stack: false
    .vgpr_count:     23
    .vgpr_spill_count: 0
    .wavefront_size: 64
  - .agpr_count:     0
    .args:
      - .address_space:  global
        .offset:         0
        .size:           8
        .value_kind:     global_buffer
      - .offset:         8
        .size:           4
        .value_kind:     by_value
      - .address_space:  global
        .offset:         16
        .size:           8
        .value_kind:     global_buffer
      - .offset:         24
        .size:           4
        .value_kind:     by_value
      - .actual_access:  write_only
        .address_space:  global
        .offset:         32
        .size:           8
        .value_kind:     global_buffer
      - .offset:         40
        .size:           4
        .value_kind:     by_value
      - .actual_access:  read_only
        .address_space:  global
        .offset:         48
        .size:           8
        .value_kind:     global_buffer
    .group_segment_fixed_size: 0
    .kernarg_segment_align: 8
    .kernarg_segment_size: 56
    .language:       OpenCL C
    .language_version:
      - 2
      - 0
    .max_flat_workgroup_size: 512
    .name:           _Z9tg_kernelILi64ELi8ELi3ELb0EEvPKDF16_iS1_iPviPKf
    .private_segment_fixed_size: 0
    .sgpr_count:     26
    .sgpr_spill_count: 0
    .symbol:         _Z9tg_kernelILi64ELi8ELi3ELb0EEvPKDF16_iS1_iPviPKf.kd
    .uniform_work_group_size: 1
    .uses_dynamic_stack: false
    .vgpr_count:     62
    .vgpr_spill_count: 0
    .wavefront_size: 64
  - .agpr_count:     0
    .args:
      - .offset:         0
        .size:           32
        .value_kind:     by_value
      - .offset:         32
        .size:           32
        .value_kind:     by_value
      - .offset:         64
        .size:           16
        .value_kind:     by_value
      - .offset:         80
        .size:           24
        .value_kind:     by_value
      - .offset:         104
        .size:           24
        .value_kind:     by_value
      - .offset:         128
        .size:           4
        .value_kind:     hidden_block_count_x
      - .offset:         132
        .size:           4
        .value_kind:     hidden_block_count_y
      - .offset:         136
        .size:           4
        .value_kind:     hidden_block_count_z
      - .offset:         140
        .size:           2
        .value_kind:     hidden_group_size_x
      - .offset:         142
        .size:           2
        .value_kind:     hidden_group_size_y
      - .offset:         144
        .size:           2
        .value_kind:     hidden_group_size_z
      - .offset:         146
        .size:           2
        .value_kind:     hidden_remainder_x
      - .offset:         148
        .size:           2
        .value_kind:     hidden_remainder_y
      - .offset:         150
        .size:           2
        .value_kind:     hidden_remainder_z
      - .offset:         168
        .size:           8
        .value_kind:     hidden_global_offset_x
      - .offset:         176
        .size:           8
        .value_kind:     hidden_global_offset_y
      - .offset:         184
        .size:           8
        .value_kind:     hidden_global_offset_z
      - .offset:         192
        .size:           2
        .value_kind:     hidden_grid_dims
      - .offset:         248
        .size:           4
        .value_kind:     hidden_dynamic_lds_size
    .group_segment_fixed_size: 0
    .kernarg_segment_align: 8
    .kernarg_segment_size: 384
    .language:       OpenCL C
    .language_version:
      - 2
      - 0
    .max_flat_workgroup_size: 512
    .name:           _Z14k_phase_gen_utIN3pg86EpiH16ILb0ELb1EEENS1_ILb1ELb0EEEEvNS0_4GemmES4_NS0_6GenSrcET_T0_
    .private_segment_fixed_size: 0
    .sgpr_count:     89
    .sgpr_spill_count: 0
    .symbol:         _Z14k_phase_gen_utIN3pg86EpiH16ILb0ELb1EEENS1_ILb1ELb0EEEEvNS0_4GemmES4_NS0_6GenSrcET_T0_.kd
    .uniform_work_group_size: 1
    .uses_dynamic_stack: false
    .vgpr_count:     252
    .vgpr_spill_count: 0
    .wavefront_size: 64
  - .agpr_count:     0
    .args:
      - .address_space:  global
        .offset:         0
        .size:           8
        .value_kind:     global_buffer
      - .offset:         8
        .size:           4
        .value_kind:     by_value
      - .address_space:  global
        .offset:         16
        .size:           8
        .value_kind:     global_buffer
      - .offset:         24
        .size:           4
        .value_kind:     by_value
      - .actual_access:  write_only
        .address_space:  global
        .offset:         32
        .size:           8
        .value_kind:     global_buffer
      - .offset:         40
        .size:           4
        .value_kind:     by_value
      - .actual_access:  read_only
        .address_space:  global
        .offset:         48
        .size:           8
        .value_kind:     global_buffer
      - .offset:         56
        .size:           4
        .value_kind:     hidden_block_count_x
      - .offset:         60
        .size:           4
        .value_kind:     hidden_block_count_y
      - .offset:         64
        .size:           4
        .value_kind:     hidden_block_count_z
      - .offset:         68
        .size:           2
        .value_kind:     hidden_group_size_x
      - .offset:         70
        .size:           2
        .value_kind:     hidden_group_size_y
      - .offset:         72
        .size:           2
        .value_kind:     hidden_group_size_z
      - .offset:         74
        .size:           2
        .value_kind:     hidden_remainder_x
      - .offset:         76
        .size:           2
        .value_kind:     hidden_remainder_y
      - .offset:         78
        .size:           2
        .value_kind:     hidden_remainder_z
      - .offset:         96
        .size:           8
        .value_kind:     hidden_global_offset_x
      - .offset:         104
        .size:           8
        .value_kind:     hidden_global_offset_y
      - .offset:         112
        .size:           8
        .value_kind:     hidden_global_offset_z
      - .offset:         120
        .size:           2
        .value_kind:     hidden_grid_dims
      - .offset:         176
        .size:           4
        .value_kind:     hidden_dynamic_lds_size
    .group_segment_fixed_size: 0
    .kernarg_segment_align: 8
    .kernarg_segment_size: 312
    .language:       OpenCL C
    .language_version:
      - 2
      - 0
    .max_flat_workgroup_size: 512
    .name:           _Z9tg_kernelILi128ELi8ELi1ELb1EEvPKDF16_iS1_iPviPKf
    .private_segment_fixed_size: 0
    .sgpr_count:     25
    .sgpr_spill_count: 0
    .symbol:         _Z9tg_kernelILi128ELi8ELi1ELb1EEvPKDF16_iS1_iPviPKf.kd
    .uniform_work_group_size: 1
    .uses_dynamic_stack: false
    .vgpr_count:     96
    .vgpr_spill_count: 0
    .wavefront_size: 64
  - .agpr_count:     0
    .args:
      - .address_space:  global
        .offset:         0
        .size:           8
        .value_kind:     global_buffer
      - .offset:         8
        .size:           4
        .value_kind:     by_value
      - .address_space:  global
        .offset:         16
        .size:           8
        .value_kind:     global_buffer
      - .offset:         24
        .size:           4
        .value_kind:     by_value
      - .actual_access:  write_only
        .address_space:  global
        .offset:         32
        .size:           8
        .value_kind:     global_buffer
      - .offset:         40
        .size:           4
        .value_kind:     by_value
      - .actual_access:  read_only
        .address_space:  global
        .offset:         48
        .size:           8
        .value_kind:     global_buffer
    .group_segment_fixed_size: 73728
    .kernarg_segment_align: 8
    .kernarg_segment_size: 56
    .language:       OpenCL C
    .language_version:
      - 2
      - 0
    .max_flat_workgroup_size: 512
    .name:           _Z9tg_kernelILi64ELi8ELi1ELb0EEvPKDF16_iS1_iPviPKf
    .private_segment_fixed_size: 0
    .sgpr_count:     38
    .sgpr_spill_count: 0
    .symbol:         _Z9tg_kernelILi64ELi8ELi1ELb0EEvPKDF16_iS1_iPviPKf.kd
    .uniform_work_group_size: 1
    .uses_dynamic_stack: false
    .vgpr_count:     128
    .vgpr_spill_count: 0
    .wavefront_size: 64
  - .agpr_count:     0
    .args:
      - .address_space:  global
        .offset:         0
        .size:           8
        .value_kind:     global_buffer
      - .offset:         8
        .size:           4
        .value_kind:     by_value
      - .address_space:  global
        .offset:         16
        .size:           8
        .value_kind:     global_buffer
      - .offset:         24
        .size:           4
        .value_kind:     by_value
      - .actual_access:  write_only
        .address_space:  global
        .offset:         32
        .size:           8
        .value_kind:     global_buffer
      - .offset:         40
        .size:           4
        .value_kind:     by_value
      - .actual_access:  read_only
        .address_space:  global
        .offset:         48
        .size:           8
        .value_kind:     global_buffer
    .group_segment_fixed_size: 0
    .kernarg_segment_align: 8
    .kernarg_segment_size: 56
    .language:       OpenCL C
    .language_version:
      - 2
      - 0
    .max_flat_workgroup_size: 512
    .name:           _Z9tg_kernelILi64ELi8ELi4ELb0EEvPKDF16_iS1_iPviPKf
    .private_segment_fixed_size: 0
    .sgpr_count:     26
    .sgpr_spill_count: 0
    .symbol:         _Z9tg_kernelILi64ELi8ELi4ELb0EEvPKDF16_iS1_iPviPKf.kd
    .uniform_work_group_size: 1
    .uses_dynamic_stack: false
    .vgpr_count:     64
    .vgpr_spill_count: 0
    .wavefront_size: 64
  - .agpr_count:     0
    .args:
      - .address_space:  global
        .offset:         0
        .size:           8
        .value_kind:     global_buffer
      - .offset:         8
        .size:           4
        .value_kind:     by_value
      - .address_space:  global
        .offset:         16
        .size:           8
        .value_kind:     global_buffer
      - .offset:         24
        .size:           4
        .value_kind:     by_value
      - .actual_access:  write_only
        .address_space:  global
        .offset:         32
        .size:           8
        .value_kind:     global_buffer
      - .offset:         40
        .size:           4
        .value_kind:     by_value
      - .actual_access:  read_only
        .address_space:  global
        .offset:         48
        .size:           8
        .value_kind:     global_buffer
    .group_segment_fixed_size: 0
    .kernarg_segment_align: 8
    .kernarg_segment_size: 56
    .language:       OpenCL C
    .language_version:
      - 2
      - 0
    .max_flat_workgroup_size: 512
    .name:           _Z9tg_kernelILi64ELi8ELi2ELb0EEvPKDF16_iS1_iPviPKf
    .private_segment_fixed_size: 0
    .sgpr_count:     22
    .sgpr_spill_count: 0
    .symbol:         _Z9tg_kernelILi64ELi8ELi2ELb0EEvPKDF16_iS1_iPviPKf.kd
    .uniform_work_group_size: 1
    .uses_dynamic_stack: false
    .vgpr_count:     62
    .vgpr_spill_count: 0
    .wavefront_size: 64
